# dispatch: the 16 serialized per-thread loads of the workgroup counter table issued together and reduced afterwards; rest as previous version
# baseline (speedup 1.0000x reference)
; #define LAS __attribute__((address_space(3)))
; __global__ void __launch_bounds__(NTHR, 2) mk_fwd(Args args) {
;     ...
;                 LAS int* sc = (LAS int*)lds; const int e = tid & 31, part = tid >> 5, per = (G + 15) >> 4;
;                 int tot = 0, off = 0;
;                 for (int j = 0; j < per; ++j) { const int w = part * per + j; if (w < G) { const int cc = wgcnt[w * 32 + e]; tot += cc; if (w < bx) off += cc; } }
;                 sc[part * 32 + e] = tot; sc[512 + part * 32 + e] = off;
.LBB0_760:
	s_cmp_lt_i32 s42, 7
	s_cselect_b64 s[8:9], -1, 0
	s_and_b64 s[8:9], s[8:9], s[6:7]
	s_andn2_b64 vcc, exec, s[8:9]
	s_cbranch_vccnz .LBB0_814
	v_mov_b32_e32 v6, v0
	s_mov_b64 s[6:7], s[0:1]
	s_load_dwordx2 s[10:11], s[6:7], 0xd8
	s_add_i32 s6, s64, 15
	s_ashr_i32 s14, s6, 4
	s_cmp_lt_i32 s14, 1
	v_and_b32_e32 v1, 31, v6
	s_cbranch_scc1 .LBB0_766
	v_ashrrev_i32_e32 v2, 5, v6
	s_waitcnt lgkmcnt(0)
	s_add_u32 s6, s10, 0x8000
	v_mul_lo_u32 v7, v2, s14
	s_addc_u32 s7, s11, 0
	v_lshl_or_b32 v2, v7, 5, v1
	v_mov_b32_e32 v4, 0
	v_mov_b32_e32 v5, 0
	v_ashrrev_i32_e32 v3, 31, v2
	v_lshl_add_u64 v[8:9], v[2:3], 2, s[6:7]
	global_load_dword v10, v[8:9], off
	global_load_dword v11, v[8:9], off offset:128
	global_load_dword v12, v[8:9], off offset:256
	global_load_dword v13, v[8:9], off offset:384
	global_load_dword v14, v[8:9], off offset:512
	global_load_dword v15, v[8:9], off offset:640
	global_load_dword v16, v[8:9], off offset:768
	global_load_dword v17, v[8:9], off offset:896
	global_load_dword v18, v[8:9], off offset:1024
	global_load_dword v19, v[8:9], off offset:1152
	global_load_dword v20, v[8:9], off offset:1280
	global_load_dword v21, v[8:9], off offset:1408
	global_load_dword v22, v[8:9], off offset:1536
	global_load_dword v23, v[8:9], off offset:1664
	global_load_dword v24, v[8:9], off offset:1792
	global_load_dword v25, v[8:9], off offset:1920
	s_waitcnt vmcnt(0)
	v_add_u32_e32 v26, 0, v7
	s_cmp_gt_i32 s14, 0
	s_cselect_b64 s[12:13], -1, 0
	v_cmp_gt_i32_e32 vcc, s64, v26
	s_and_b64 vcc, vcc, s[12:13]
	s_nop 1
	v_cndmask_b32_e32 v27, 0, v10, vcc
	v_add_u32_e32 v4, v27, v4
	v_cmp_gt_i32_e32 vcc, s2, v26
	s_nop 1
	v_cndmask_b32_e32 v27, 0, v27, vcc
	v_add_u32_e32 v5, v27, v5
	v_add_u32_e32 v26, 1, v7
	s_cmp_gt_i32 s14, 1
	s_cselect_b64 s[12:13], -1, 0
	v_cmp_gt_i32_e32 vcc, s64, v26
	s_and_b64 vcc, vcc, s[12:13]
	s_nop 1
	v_cndmask_b32_e32 v27, 0, v11, vcc
	v_add_u32_e32 v4, v27, v4
	v_cmp_gt_i32_e32 vcc, s2, v26
	s_nop 1
	v_cndmask_b32_e32 v27, 0, v27, vcc
	v_add_u32_e32 v5, v27, v5
	v_add_u32_e32 v26, 2, v7
	s_cmp_gt_i32 s14, 2
	s_cselect_b64 s[12:13], -1, 0
	v_cmp_gt_i32_e32 vcc, s64, v26
	s_and_b64 vcc, vcc, s[12:13]
	s_nop 1
	v_cndmask_b32_e32 v27, 0, v12, vcc
	v_add_u32_e32 v4, v27, v4
	v_cmp_gt_i32_e32 vcc, s2, v26
	s_nop 1
	v_cndmask_b32_e32 v27, 0, v27, vcc
	v_add_u32_e32 v5, v27, v5
	v_add_u32_e32 v26, 3, v7
	s_cmp_gt_i32 s14, 3
	s_cselect_b64 s[12:13], -1, 0
	v_cmp_gt_i32_e32 vcc, s64, v26
	s_and_b64 vcc, vcc, s[12:13]
	s_nop 1
	v_cndmask_b32_e32 v27, 0, v13, vcc
	v_add_u32_e32 v4, v27, v4
	v_cmp_gt_i32_e32 vcc, s2, v26
	s_nop 1
	v_cndmask_b32_e32 v27, 0, v27, vcc
	v_add_u32_e32 v5, v27, v5
	v_add_u32_e32 v26, 4, v7
	s_cmp_gt_i32 s14, 4
	s_cselect_b64 s[12:13], -1, 0
	v_cmp_gt_i32_e32 vcc, s64, v26
	s_and_b64 vcc, vcc, s[12:13]
	s_nop 1
	v_cndmask_b32_e32 v27, 0, v14, vcc
	v_add_u32_e32 v4, v27, v4
	v_cmp_gt_i32_e32 vcc, s2, v26
	s_nop 1
	v_cndmask_b32_e32 v27, 0, v27, vcc
	v_add_u32_e32 v5, v27, v5
	v_add_u32_e32 v26, 5, v7
	s_cmp_gt_i32 s14, 5
	s_cselect_b64 s[12:13], -1, 0
	v_cmp_gt_i32_e32 vcc, s64, v26
	s_and_b64 vcc, vcc, s[12:13]
	s_nop 1
	v_cndmask_b32_e32 v27, 0, v15, vcc
	v_add_u32_e32 v4, v27, v4
	v_cmp_gt_i32_e32 vcc, s2, v26
	s_nop 1
	v_cndmask_b32_e32 v27, 0, v27, vcc
	v_add_u32_e32 v5, v27, v5
	v_add_u32_e32 v26, 6, v7
	s_cmp_gt_i32 s14, 6
	s_cselect_b64 s[12:13], -1, 0
	v_cmp_gt_i32_e32 vcc, s64, v26
	s_and_b64 vcc, vcc, s[12:13]
	s_nop 1
	v_cndmask_b32_e32 v27, 0, v16, vcc
	v_add_u32_e32 v4, v27, v4
	v_cmp_gt_i32_e32 vcc, s2, v26
	s_nop 1
	v_cndmask_b32_e32 v27, 0, v27, vcc
	v_add_u32_e32 v5, v27, v5
	v_add_u32_e32 v26, 7, v7
	s_cmp_gt_i32 s14, 7
	s_cselect_b64 s[12:13], -1, 0
	v_cmp_gt_i32_e32 vcc, s64, v26
	s_and_b64 vcc, vcc, s[12:13]
	s_nop 1
	v_cndmask_b32_e32 v27, 0, v17, vcc
	v_add_u32_e32 v4, v27, v4
	v_cmp_gt_i32_e32 vcc, s2, v26
	s_nop 1
	v_cndmask_b32_e32 v27, 0, v27, vcc
	v_add_u32_e32 v5, v27, v5
	v_add_u32_e32 v26, 8, v7
	s_cmp_gt_i32 s14, 8
	s_cselect_b64 s[12:13], -1, 0
	v_cmp_gt_i32_e32 vcc, s64, v26
	s_and_b64 vcc, vcc, s[12:13]
	s_nop 1
	v_cndmask_b32_e32 v27, 0, v18, vcc
	v_add_u32_e32 v4, v27, v4
	v_cmp_gt_i32_e32 vcc, s2, v26
	s_nop 1
	v_cndmask_b32_e32 v27, 0, v27, vcc
	v_add_u32_e32 v5, v27, v5
	v_add_u32_e32 v26, 9, v7
	s_cmp_gt_i32 s14, 9
	s_cselect_b64 s[12:13], -1, 0
	v_cmp_gt_i32_e32 vcc, s64, v26
	s_and_b64 vcc, vcc, s[12:13]
	s_nop 1
	v_cndmask_b32_e32 v27, 0, v19, vcc
	v_add_u32_e32 v4, v27, v4
	v_cmp_gt_i32_e32 vcc, s2, v26
	s_nop 1
	v_cndmask_b32_e32 v27, 0, v27, vcc
	v_add_u32_e32 v5, v27, v5
	v_add_u32_e32 v26, 10, v7
	s_cmp_gt_i32 s14, 10
	s_cselect_b64 s[12:13], -1, 0
	v_cmp_gt_i32_e32 vcc, s64, v26
	s_and_b64 vcc, vcc, s[12:13]
	s_nop 1
	v_cndmask_b32_e32 v27, 0, v20, vcc
	v_add_u32_e32 v4, v27, v4
	v_cmp_gt_i32_e32 vcc, s2, v26
	s_nop 1
	v_cndmask_b32_e32 v27, 0, v27, vcc
	v_add_u32_e32 v5, v27, v5
	v_add_u32_e32 v26, 11, v7
	s_cmp_gt_i32 s14, 11
	s_cselect_b64 s[12:13], -1, 0
	v_cmp_gt_i32_e32 vcc, s64, v26
	s_and_b64 vcc, vcc, s[12:13]
	s_nop 1
	v_cndmask_b32_e32 v27, 0, v21, vcc
	v_add_u32_e32 v4, v27, v4
	v_cmp_gt_i32_e32 vcc, s2, v26
	s_nop 1
	v_cndmask_b32_e32 v27, 0, v27, vcc
	v_add_u32_e32 v5, v27, v5
	v_add_u32_e32 v26, 12, v7
	s_cmp_gt_i32 s14, 12
	s_cselect_b64 s[12:13], -1, 0
	v_cmp_gt_i32_e32 vcc, s64, v26
	s_and_b64 vcc, vcc, s[12:13]
	s_nop 1
	v_cndmask_b32_e32 v27, 0, v22, vcc
	v_add_u32_e32 v4, v27, v4
	v_cmp_gt_i32_e32 vcc, s2, v26
	s_nop 1
	v_cndmask_b32_e32 v27, 0, v27, vcc
	v_add_u32_e32 v5, v27, v5
	v_add_u32_e32 v26, 13, v7
	s_cmp_gt_i32 s14, 13
	s_cselect_b64 s[12:13], -1, 0
	v_cmp_gt_i32_e32 vcc, s64, v26
	s_and_b64 vcc, vcc, s[12:13]
	s_nop 1
	v_cndmask_b32_e32 v27, 0, v23, vcc
	v_add_u32_e32 v4, v27, v4
	v_cmp_gt_i32_e32 vcc, s2, v26
	s_nop 1
	v_cndmask_b32_e32 v27, 0, v27, vcc
	v_add_u32_e32 v5, v27, v5
	v_add_u32_e32 v26, 14, v7
	s_cmp_gt_i32 s14, 14
	s_cselect_b64 s[12:13], -1, 0
	v_cmp_gt_i32_e32 vcc, s64, v26
	s_and_b64 vcc, vcc, s[12:13]
	s_nop 1
	v_cndmask_b32_e32 v27, 0, v24, vcc
	v_add_u32_e32 v4, v27, v4
	v_cmp_gt_i32_e32 vcc, s2, v26
	s_nop 1
	v_cndmask_b32_e32 v27, 0, v27, vcc
	v_add_u32_e32 v5, v27, v5
	v_add_u32_e32 v26, 15, v7
	s_cmp_gt_i32 s14, 15
	s_cselect_b64 s[12:13], -1, 0
	v_cmp_gt_i32_e32 vcc, s64, v26
	s_and_b64 vcc, vcc, s[12:13]
	s_nop 1
	v_cndmask_b32_e32 v27, 0, v25, vcc
	v_add_u32_e32 v4, v27, v4
	v_cmp_gt_i32_e32 vcc, s2, v26
	s_nop 1
	v_cndmask_b32_e32 v27, 0, v27, vcc
	v_add_u32_e32 v5, v27, v5
	s_branch .LBB0_767

; #define LAS __attribute__((address_space(3)))
; __global__ void __launch_bounds__(NTHR, 2) mk_fwd(Args args) {
;     ...
;                 LAS int* sc = (LAS int*)lds; const int e = tid & 31, part = tid >> 5, per = (G + 15) >> 4;
;                 int tot = 0, off = 0;
;                 for (int j = 0; j < per; ++j) { const int w = part * per + j; if (w < G) { const int cc = wgcnt[w * 32 + e]; tot += cc; if (w < bx) off += cc; } }
;                 sc[part * 32 + e] = tot; sc[512 + part * 32 + e] = off;
.LBB0_1665:
	s_cmp_lt_i32 s42, 16
	s_cselect_b64 s[6:7], -1, 0
	s_and_b64 s[6:7], s[6:7], s[4:5]
	s_andn2_b64 vcc, exec, s[6:7]
	s_cbranch_vccnz .LBB0_1717
	s_waitcnt vmcnt(0)
	v_mov_b32_e32 v6, v0
	s_mov_b64 s[4:5], s[0:1]
	s_waitcnt lgkmcnt(0)
	s_load_dwordx2 s[8:9], s[4:5], 0xd8
	s_add_i32 s4, s64, 15
	s_ashr_i32 s12, s4, 4
	s_cmp_lt_i32 s12, 1
	v_and_b32_e32 v1, 31, v6
	s_cbranch_scc1 .LBB0_1671
	v_ashrrev_i32_e32 v2, 5, v6
	s_waitcnt lgkmcnt(0)
	s_add_u32 s4, s8, 0x10000
	v_mul_lo_u32 v7, v2, s12
	s_addc_u32 s5, s9, 0
	v_lshl_or_b32 v2, v7, 5, v1
	v_mov_b32_e32 v4, 0
	v_mov_b32_e32 v5, 0
	v_ashrrev_i32_e32 v3, 31, v2
	v_lshl_add_u64 v[8:9], v[2:3], 2, s[4:5]
	global_load_dword v10, v[8:9], off
	global_load_dword v11, v[8:9], off offset:128
	global_load_dword v12, v[8:9], off offset:256
	global_load_dword v13, v[8:9], off offset:384
	global_load_dword v14, v[8:9], off offset:512
	global_load_dword v15, v[8:9], off offset:640
	global_load_dword v16, v[8:9], off offset:768
	global_load_dword v17, v[8:9], off offset:896
	global_load_dword v18, v[8:9], off offset:1024
	global_load_dword v19, v[8:9], off offset:1152
	global_load_dword v20, v[8:9], off offset:1280
	global_load_dword v21, v[8:9], off offset:1408
	global_load_dword v22, v[8:9], off offset:1536
	global_load_dword v23, v[8:9], off offset:1664
	global_load_dword v24, v[8:9], off offset:1792
	global_load_dword v25, v[8:9], off offset:1920
	s_waitcnt vmcnt(0)
	v_add_u32_e32 v26, 0, v7
	s_cmp_gt_i32 s12, 0
	s_cselect_b64 s[10:11], -1, 0
	v_cmp_gt_i32_e32 vcc, s64, v26
	s_and_b64 vcc, vcc, s[10:11]
	s_nop 1
	v_cndmask_b32_e32 v27, 0, v10, vcc
	v_add_u32_e32 v4, v27, v4
	v_cmp_gt_i32_e32 vcc, s2, v26
	s_nop 1
	v_cndmask_b32_e32 v27, 0, v27, vcc
	v_add_u32_e32 v5, v27, v5
	v_add_u32_e32 v26, 1, v7
	s_cmp_gt_i32 s12, 1
	s_cselect_b64 s[10:11], -1, 0
	v_cmp_gt_i32_e32 vcc, s64, v26
	s_and_b64 vcc, vcc, s[10:11]
	s_nop 1
	v_cndmask_b32_e32 v27, 0, v11, vcc
	v_add_u32_e32 v4, v27, v4
	v_cmp_gt_i32_e32 vcc, s2, v26
	s_nop 1
	v_cndmask_b32_e32 v27, 0, v27, vcc
	v_add_u32_e32 v5, v27, v5
	v_add_u32_e32 v26, 2, v7
	s_cmp_gt_i32 s12, 2
	s_cselect_b64 s[10:11], -1, 0
	v_cmp_gt_i32_e32 vcc, s64, v26
	s_and_b64 vcc, vcc, s[10:11]
	s_nop 1
	v_cndmask_b32_e32 v27, 0, v12, vcc
	v_add_u32_e32 v4, v27, v4
	v_cmp_gt_i32_e32 vcc, s2, v26
	s_nop 1
	v_cndmask_b32_e32 v27, 0, v27, vcc
	v_add_u32_e32 v5, v27, v5
	v_add_u32_e32 v26, 3, v7
	s_cmp_gt_i32 s12, 3
	s_cselect_b64 s[10:11], -1, 0
	v_cmp_gt_i32_e32 vcc, s64, v26
	s_and_b64 vcc, vcc, s[10:11]
	s_nop 1
	v_cndmask_b32_e32 v27, 0, v13, vcc
	v_add_u32_e32 v4, v27, v4
	v_cmp_gt_i32_e32 vcc, s2, v26
	s_nop 1
	v_cndmask_b32_e32 v27, 0, v27, vcc
	v_add_u32_e32 v5, v27, v5
	v_add_u32_e32 v26, 4, v7
	s_cmp_gt_i32 s12, 4
	s_cselect_b64 s[10:11], -1, 0
	v_cmp_gt_i32_e32 vcc, s64, v26
	s_and_b64 vcc, vcc, s[10:11]
	s_nop 1
	v_cndmask_b32_e32 v27, 0, v14, vcc
	v_add_u32_e32 v4, v27, v4
	v_cmp_gt_i32_e32 vcc, s2, v26
	s_nop 1
	v_cndmask_b32_e32 v27, 0, v27, vcc
	v_add_u32_e32 v5, v27, v5
	v_add_u32_e32 v26, 5, v7
	s_cmp_gt_i32 s12, 5
	s_cselect_b64 s[10:11], -1, 0
	v_cmp_gt_i32_e32 vcc, s64, v26
	s_and_b64 vcc, vcc, s[10:11]
	s_nop 1
	v_cndmask_b32_e32 v27, 0, v15, vcc
	v_add_u32_e32 v4, v27, v4
	v_cmp_gt_i32_e32 vcc, s2, v26
	s_nop 1
	v_cndmask_b32_e32 v27, 0, v27, vcc
	v_add_u32_e32 v5, v27, v5
	v_add_u32_e32 v26, 6, v7
	s_cmp_gt_i32 s12, 6
	s_cselect_b64 s[10:11], -1, 0
	v_cmp_gt_i32_e32 vcc, s64, v26
	s_and_b64 vcc, vcc, s[10:11]
	s_nop 1
	v_cndmask_b32_e32 v27, 0, v16, vcc
	v_add_u32_e32 v4, v27, v4
	v_cmp_gt_i32_e32 vcc, s2, v26
	s_nop 1
	v_cndmask_b32_e32 v27, 0, v27, vcc
	v_add_u32_e32 v5, v27, v5
	v_add_u32_e32 v26, 7, v7
	s_cmp_gt_i32 s12, 7
	s_cselect_b64 s[10:11], -1, 0
	v_cmp_gt_i32_e32 vcc, s64, v26
	s_and_b64 vcc, vcc, s[10:11]
	s_nop 1
	v_cndmask_b32_e32 v27, 0, v17, vcc
	v_add_u32_e32 v4, v27, v4
	v_cmp_gt_i32_e32 vcc, s2, v26
	s_nop 1
	v_cndmask_b32_e32 v27, 0, v27, vcc
	v_add_u32_e32 v5, v27, v5
	v_add_u32_e32 v26, 8, v7
	s_cmp_gt_i32 s12, 8
	s_cselect_b64 s[10:11], -1, 0
	v_cmp_gt_i32_e32 vcc, s64, v26
	s_and_b64 vcc, vcc, s[10:11]
	s_nop 1
	v_cndmask_b32_e32 v27, 0, v18, vcc
	v_add_u32_e32 v4, v27, v4
	v_cmp_gt_i32_e32 vcc, s2, v26
	s_nop 1
	v_cndmask_b32_e32 v27, 0, v27, vcc
	v_add_u32_e32 v5, v27, v5
	v_add_u32_e32 v26, 9, v7
	s_cmp_gt_i32 s12, 9
	s_cselect_b64 s[10:11], -1, 0
	v_cmp_gt_i32_e32 vcc, s64, v26
	s_and_b64 vcc, vcc, s[10:11]
	s_nop 1
	v_cndmask_b32_e32 v27, 0, v19, vcc
	v_add_u32_e32 v4, v27, v4
	v_cmp_gt_i32_e32 vcc, s2, v26
	s_nop 1
	v_cndmask_b32_e32 v27, 0, v27, vcc
	v_add_u32_e32 v5, v27, v5
	v_add_u32_e32 v26, 10, v7
	s_cmp_gt_i32 s12, 10
	s_cselect_b64 s[10:11], -1, 0
	v_cmp_gt_i32_e32 vcc, s64, v26
	s_and_b64 vcc, vcc, s[10:11]
	s_nop 1
	v_cndmask_b32_e32 v27, 0, v20, vcc
	v_add_u32_e32 v4, v27, v4
	v_cmp_gt_i32_e32 vcc, s2, v26
	s_nop 1
	v_cndmask_b32_e32 v27, 0, v27, vcc
	v_add_u32_e32 v5, v27, v5
	v_add_u32_e32 v26, 11, v7
	s_cmp_gt_i32 s12, 11
	s_cselect_b64 s[10:11], -1, 0
	v_cmp_gt_i32_e32 vcc, s64, v26
	s_and_b64 vcc, vcc, s[10:11]
	s_nop 1
	v_cndmask_b32_e32 v27, 0, v21, vcc
	v_add_u32_e32 v4, v27, v4
	v_cmp_gt_i32_e32 vcc, s2, v26
	s_nop 1
	v_cndmask_b32_e32 v27, 0, v27, vcc
	v_add_u32_e32 v5, v27, v5
	v_add_u32_e32 v26, 12, v7
	s_cmp_gt_i32 s12, 12
	s_cselect_b64 s[10:11], -1, 0
	v_cmp_gt_i32_e32 vcc, s64, v26
	s_and_b64 vcc, vcc, s[10:11]
	s_nop 1
	v_cndmask_b32_e32 v27, 0, v22, vcc
	v_add_u32_e32 v4, v27, v4
	v_cmp_gt_i32_e32 vcc, s2, v26
	s_nop 1
	v_cndmask_b32_e32 v27, 0, v27, vcc
	v_add_u32_e32 v5, v27, v5
	v_add_u32_e32 v26, 13, v7
	s_cmp_gt_i32 s12, 13
	s_cselect_b64 s[10:11], -1, 0
	v_cmp_gt_i32_e32 vcc, s64, v26
	s_and_b64 vcc, vcc, s[10:11]
	s_nop 1
	v_cndmask_b32_e32 v27, 0, v23, vcc
	v_add_u32_e32 v4, v27, v4
	v_cmp_gt_i32_e32 vcc, s2, v26
	s_nop 1
	v_cndmask_b32_e32 v27, 0, v27, vcc
	v_add_u32_e32 v5, v27, v5
	v_add_u32_e32 v26, 14, v7
	s_cmp_gt_i32 s12, 14
	s_cselect_b64 s[10:11], -1, 0
	v_cmp_gt_i32_e32 vcc, s64, v26
	s_and_b64 vcc, vcc, s[10:11]
	s_nop 1
	v_cndmask_b32_e32 v27, 0, v24, vcc
	v_add_u32_e32 v4, v27, v4
	v_cmp_gt_i32_e32 vcc, s2, v26
	s_nop 1
	v_cndmask_b32_e32 v27, 0, v27, vcc
	v_add_u32_e32 v5, v27, v5
	v_add_u32_e32 v26, 15, v7
	s_cmp_gt_i32 s12, 15
	s_cselect_b64 s[10:11], -1, 0
	v_cmp_gt_i32_e32 vcc, s64, v26
	s_and_b64 vcc, vcc, s[10:11]
	s_nop 1
	v_cndmask_b32_e32 v27, 0, v25, vcc
	v_add_u32_e32 v4, v27, v4
	v_cmp_gt_i32_e32 vcc, s2, v26
	s_nop 1
	v_cndmask_b32_e32 v27, 0, v27, vcc
	v_add_u32_e32 v5, v27, v5
	s_branch .LBB0_1672
